# P6 router: weight fragments loaded once per chunk into spare registers, per-group MFMA loop unrolled with pipelined LDS reads
# baseline (speedup 1.0000x reference)
.LBB0_587:
	s_and_saveexec_b64 s[0:1], s[4:5]
	ds_write_b32 v157, v73
	s_or_b64 exec, exec, s[0:1]
	s_lshl_b32 s43, s42, 7
	s_mov_b32 s85, 0
	s_waitcnt lgkmcnt(0)
	s_barrier
	global_load_dwordx4 v[186:189], v[78:79], off offset:-64
	global_load_dwordx4 v[190:193], v[78:79], off offset:-32
	global_load_dwordx4 v[194:197], v[78:79], off
	global_load_dwordx4 v[198:201], v[78:79], off offset:32
	global_load_dwordx4 v[202:205], v[78:79], off offset:64
	global_load_dwordx4 v[206:209], v[78:79], off offset:96
	global_load_dwordx4 v[210:213], v[78:79], off offset:128
	global_load_dwordx4 v[214:217], v[78:79], off offset:160
	global_load_dwordx4 v[218:221], v[78:79], off offset:192
	global_load_dwordx4 v[222:225], v[78:79], off offset:224
	global_load_dwordx4 v[226:229], v[78:79], off offset:256
	global_load_dwordx4 v[230:233], v[78:79], off offset:288
	global_load_dwordx4 v[236:239], v[78:79], off offset:320
	global_load_dwordx4 v[240:243], v[78:79], off offset:352
	global_load_dwordx4 v[244:247], v[78:79], off offset:384
	global_load_dwordx4 v[248:251], v[78:79], off offset:416
	s_branch .LBB0_591

.LBB0_592:
	ds_read_b128 v[80:83], v166
	ds_read_b128 v[84:87], v166 offset:1024
	ds_read_b128 v[56:59], v166 offset:2048
	ds_read_b128 v[60:63], v166 offset:3072
	s_waitcnt lgkmcnt(3)
	v_mfma_f32_32x32x16_bf16 v[2:17], v[80:83], v[186:189], v[2:17]
	ds_read_b128 v[80:83], v166 offset:4096
	s_waitcnt lgkmcnt(3)
	v_mfma_f32_32x32x16_bf16 v[2:17], v[84:87], v[190:193], v[2:17]
	ds_read_b128 v[84:87], v166 offset:5120
	s_waitcnt lgkmcnt(3)
	v_mfma_f32_32x32x16_bf16 v[2:17], v[56:59], v[194:197], v[2:17]
	ds_read_b128 v[56:59], v166 offset:6144
	s_waitcnt lgkmcnt(3)
	v_mfma_f32_32x32x16_bf16 v[2:17], v[60:63], v[198:201], v[2:17]
	ds_read_b128 v[60:63], v166 offset:7168
	s_waitcnt lgkmcnt(3)
	v_mfma_f32_32x32x16_bf16 v[2:17], v[80:83], v[202:205], v[2:17]
	ds_read_b128 v[80:83], v166 offset:8192
	s_waitcnt lgkmcnt(3)
	v_mfma_f32_32x32x16_bf16 v[2:17], v[84:87], v[206:209], v[2:17]
	ds_read_b128 v[84:87], v166 offset:9216
	s_waitcnt lgkmcnt(3)
	v_mfma_f32_32x32x16_bf16 v[2:17], v[56:59], v[210:213], v[2:17]
	ds_read_b128 v[56:59], v166 offset:10240
	s_waitcnt lgkmcnt(3)
	v_mfma_f32_32x32x16_bf16 v[2:17], v[60:63], v[214:217], v[2:17]
	ds_read_b128 v[60:63], v166 offset:11264
	s_waitcnt lgkmcnt(3)
	v_mfma_f32_32x32x16_bf16 v[2:17], v[80:83], v[218:221], v[2:17]
	ds_read_b128 v[80:83], v166 offset:12288
	s_waitcnt lgkmcnt(3)
	v_mfma_f32_32x32x16_bf16 v[2:17], v[84:87], v[222:225], v[2:17]
	ds_read_b128 v[84:87], v166 offset:13312
	s_waitcnt lgkmcnt(3)
	v_mfma_f32_32x32x16_bf16 v[2:17], v[56:59], v[226:229], v[2:17]
	ds_read_b128 v[56:59], v166 offset:14336
	s_waitcnt lgkmcnt(3)
	v_mfma_f32_32x32x16_bf16 v[2:17], v[60:63], v[230:233], v[2:17]
	ds_read_b128 v[60:63], v166 offset:15360
	s_waitcnt lgkmcnt(3)
	v_mfma_f32_32x32x16_bf16 v[2:17], v[80:83], v[236:239], v[2:17]
	s_waitcnt lgkmcnt(2)
	v_mfma_f32_32x32x16_bf16 v[2:17], v[84:87], v[240:243], v[2:17]
	s_waitcnt lgkmcnt(1)
	v_mfma_f32_32x32x16_bf16 v[2:17], v[56:59], v[244:247], v[2:17]
	s_waitcnt lgkmcnt(0)
	v_mfma_f32_32x32x16_bf16 v[2:17], v[60:63], v[248:251], v[2:17]
	s_movk_i32 s0, 0x4000
	v_add_u32_e32 v0, 0x400, v167
	s_barrier
	s_nop 8
	ds_write2_b32 v167, v2, v3 offset1:33
	ds_write2_b32 v167, v4, v5 offset0:66 offset1:99
	ds_write2_b32 v0, v6, v7 offset0:8 offset1:41
	ds_write2_b32 v0, v8, v9 offset0:74 offset1:107
	v_add_u32_e32 v0, 0x800, v167
	ds_write2_b32 v0, v10, v11 offset0:16 offset1:49
	ds_write2_b32 v0, v12, v13 offset0:82 offset1:115
	v_add_u32_e32 v0, 0xc00, v167
	ds_write2_b32 v0, v14, v15 offset0:24 offset1:57
	ds_write2_b32 v0, v16, v17 offset0:90 offset1:123
	s_waitcnt lgkmcnt(0)
	s_barrier
	global_load_dwordx2 v[2:3], v[74:75], off
	v_add_u32_e32 v8, 0x2100, v168
	v_add_u32_e32 v10, 0x3180, v168
	v_add_u32_e32 v12, 0x4200, v168
	v_add_u32_e32 v14, 0x5280, v168
	v_add_u32_e32 v16, 0x6300, v168
	v_add_u32_e32 v50, 0x7380, v168
	v_add_u32_e32 v0, 0x1080, v168
	ds_read2_b32 v[4:5], v168 offset1:1
	ds_read2_b32 v[6:7], v0 offset1:1
	ds_read2_b32 v[8:9], v8 offset1:1
	ds_read2_b32 v[10:11], v10 offset1:1
	ds_read2_b32 v[12:13], v12 offset1:1
	ds_read2_b32 v[14:15], v14 offset1:1
	ds_read2_b32 v[16:17], v16 offset1:1
	ds_read2_b32 v[50:51], v50 offset1:1
	s_waitcnt lgkmcnt(7)
	v_pk_add_f32 v[4:5], v[4:5], 0 op_sel_hi:[1,0]
	s_waitcnt lgkmcnt(6)
	v_pk_add_f32 v[4:5], v[4:5], v[6:7]
	s_waitcnt lgkmcnt(5)
	v_pk_add_f32 v[4:5], v[4:5], v[8:9]
	s_waitcnt lgkmcnt(4)
	v_pk_add_f32 v[4:5], v[4:5], v[10:11]
	s_waitcnt lgkmcnt(3)
	v_pk_add_f32 v[4:5], v[4:5], v[12:13]
	s_waitcnt lgkmcnt(2)
	v_pk_add_f32 v[4:5], v[4:5], v[14:15]
	s_waitcnt lgkmcnt(1)
	v_pk_add_f32 v[4:5], v[4:5], v[16:17]
	s_waitcnt lgkmcnt(0)
	v_pk_add_f32 v[4:5], v[4:5], v[50:51]
	s_waitcnt vmcnt(0)
	v_pk_add_f32 v[2:3], v[4:5], v[2:3]
	ds_write2_b32 v165, v2, v3 offset1:1
	s_waitcnt lgkmcnt(0)
	s_barrier
	s_and_saveexec_b64 s[46:47], s[4:5]
	s_cbranch_execz .LBB0_590
	ds_read2_b32 v[2:3], v169 offset1:1
	ds_read2_b32 v[4:5], v169 offset0:2 offset1:3
	s_waitcnt lgkmcnt(1)
	v_max_f32_e32 v0, v2, v2
	v_max_f32_e32 v0, 0xff800000, v0
	v_cmp_gt_f32_e32 vcc, v3, v0
	s_nop 1
	v_cndmask_b32_e32 v0, v0, v3, vcc
	v_cndmask_b32_e64 v6, 0, 1, vcc
	s_waitcnt lgkmcnt(0)
	v_cmp_gt_f32_e32 vcc, v4, v0
	s_nop 1
	v_cndmask_b32_e32 v0, v0, v4, vcc
	v_cndmask_b32_e64 v6, v6, 2, vcc
	v_cmp_gt_f32_e32 vcc, v5, v0
	s_nop 1
	v_cndmask_b32_e64 v8, v6, 3, vcc
	ds_read2_b32 v[6:7], v169 offset0:4 offset1:5
	v_cndmask_b32_e32 v0, v0, v5, vcc
	s_waitcnt lgkmcnt(0)
	v_cmp_gt_f32_e32 vcc, v6, v0
	s_nop 1
	v_cndmask_b32_e32 v0, v0, v6, vcc
	v_cndmask_b32_e64 v8, v8, 4, vcc
	v_cmp_gt_f32_e32 vcc, v7, v0
	s_nop 1
	v_cndmask_b32_e64 v10, v8, 5, vcc
	ds_read2_b32 v[8:9], v169 offset0:6 offset1:7
	v_cndmask_b32_e32 v0, v0, v7, vcc
	s_waitcnt lgkmcnt(0)
	v_cmp_gt_f32_e32 vcc, v8, v0
	s_nop 1
	v_cndmask_b32_e32 v0, v0, v8, vcc
	v_cndmask_b32_e64 v10, v10, 6, vcc
	v_cmp_gt_f32_e32 vcc, v9, v0
	s_nop 1
	v_cndmask_b32_e64 v12, v10, 7, vcc
	ds_read2_b32 v[10:11], v169 offset0:8 offset1:9
	v_cndmask_b32_e32 v0, v0, v9, vcc
	s_waitcnt lgkmcnt(0)
	v_cmp_gt_f32_e32 vcc, v10, v0
	s_nop 1
	v_cndmask_b32_e32 v0, v0, v10, vcc
	v_cndmask_b32_e64 v12, v12, 8, vcc
	v_cmp_gt_f32_e32 vcc, v11, v0
	s_nop 1
	v_cndmask_b32_e64 v14, v12, 9, vcc
	ds_read2_b32 v[12:13], v169 offset0:10 offset1:11
	v_cndmask_b32_e32 v0, v0, v11, vcc
	s_waitcnt lgkmcnt(0)
	v_cmp_gt_f32_e32 vcc, v12, v0
	s_nop 1
	v_cndmask_b32_e32 v0, v0, v12, vcc
	v_cndmask_b32_e64 v14, v14, 10, vcc
	v_cmp_gt_f32_e32 vcc, v13, v0
	s_nop 1
	v_cndmask_b32_e64 v16, v14, 11, vcc
	ds_read2_b32 v[14:15], v169 offset0:12 offset1:13
	v_cndmask_b32_e32 v0, v0, v13, vcc
	s_waitcnt lgkmcnt(0)
	v_cmp_gt_f32_e32 vcc, v14, v0
	s_nop 1
	v_cndmask_b32_e32 v0, v0, v14, vcc
	v_cndmask_b32_e64 v16, v16, 12, vcc
	v_cmp_gt_f32_e32 vcc, v15, v0
	s_nop 1
	v_cndmask_b32_e64 v50, v16, 13, vcc
	ds_read2_b32 v[16:17], v169 offset0:14 offset1:15
	v_cndmask_b32_e32 v0, v0, v15, vcc
	s_waitcnt lgkmcnt(0)
	v_cmp_gt_f32_e32 vcc, v16, v0
	s_nop 1
	v_cndmask_b32_e32 v0, v0, v16, vcc
	v_cndmask_b32_e64 v50, v50, 14, vcc
	v_cmp_gt_f32_e32 vcc, v17, v0
	s_nop 1
	v_cndmask_b32_e64 v52, v50, 15, vcc
	ds_read2_b32 v[50:51], v169 offset0:16 offset1:17
	v_cndmask_b32_e32 v0, v0, v17, vcc
	s_waitcnt lgkmcnt(0)
	v_cmp_gt_f32_e32 vcc, v50, v0
	s_nop 1
	v_cndmask_b32_e32 v0, v0, v50, vcc
	v_cndmask_b32_e64 v52, v52, 16, vcc
	v_cmp_gt_f32_e32 vcc, v51, v0
	s_nop 1
	v_cndmask_b32_e64 v54, v52, 17, vcc
	ds_read2_b32 v[52:53], v169 offset0:18 offset1:19
	v_cndmask_b32_e32 v0, v0, v51, vcc
	s_waitcnt lgkmcnt(0)
	v_cmp_gt_f32_e32 vcc, v52, v0
	s_nop 1
	v_cndmask_b32_e32 v0, v0, v52, vcc
	v_cndmask_b32_e64 v54, v54, 18, vcc
	v_cmp_gt_f32_e32 vcc, v53, v0
	s_nop 1
	v_cndmask_b32_e64 v56, v54, 19, vcc
	ds_read2_b32 v[54:55], v169 offset0:20 offset1:21
	v_cndmask_b32_e32 v0, v0, v53, vcc
	s_waitcnt lgkmcnt(0)
	v_cmp_gt_f32_e32 vcc, v54, v0
	s_nop 1
	v_cndmask_b32_e32 v0, v0, v54, vcc
	v_cndmask_b32_e64 v56, v56, 20, vcc
	v_cmp_gt_f32_e32 vcc, v55, v0
	s_nop 1
	v_cndmask_b32_e64 v58, v56, 21, vcc
	ds_read2_b32 v[56:57], v169 offset0:22 offset1:23
	v_cndmask_b32_e32 v0, v0, v55, vcc
	s_waitcnt lgkmcnt(0)
	v_cmp_gt_f32_e32 vcc, v56, v0
	s_nop 1
	v_cndmask_b32_e32 v0, v0, v56, vcc
	v_cndmask_b32_e64 v58, v58, 22, vcc
	v_cmp_gt_f32_e32 vcc, v57, v0
	s_nop 1
	v_cndmask_b32_e64 v60, v58, 23, vcc
	ds_read2_b32 v[58:59], v169 offset0:24 offset1:25
	v_cndmask_b32_e32 v0, v0, v57, vcc
	s_waitcnt lgkmcnt(0)
	v_cmp_gt_f32_e32 vcc, v58, v0
	s_nop 1
	v_cndmask_b32_e32 v0, v0, v58, vcc
	v_cndmask_b32_e64 v60, v60, 24, vcc
	v_cmp_gt_f32_e32 vcc, v59, v0
	s_nop 1
	v_cndmask_b32_e64 v62, v60, 25, vcc
	ds_read2_b32 v[60:61], v169 offset0:26 offset1:27
	v_cndmask_b32_e32 v0, v0, v59, vcc
	s_waitcnt lgkmcnt(0)
	v_cmp_gt_f32_e32 vcc, v60, v0
	s_nop 1
	v_cndmask_b32_e32 v0, v0, v60, vcc
	v_cndmask_b32_e64 v62, v62, 26, vcc
	v_cmp_gt_f32_e32 vcc, v61, v0
	s_nop 1
	v_cndmask_b32_e64 v64, v62, 27, vcc
	ds_read2_b32 v[62:63], v169 offset0:28 offset1:29
	v_cndmask_b32_e32 v0, v0, v61, vcc
	s_waitcnt lgkmcnt(0)
	v_cmp_gt_f32_e32 vcc, v62, v0
	s_nop 1
	v_cndmask_b32_e32 v0, v0, v62, vcc
	v_cndmask_b32_e64 v64, v64, 28, vcc
	v_cmp_gt_f32_e32 vcc, v63, v0
	s_nop 1
	v_cndmask_b32_e64 v72, v64, 29, vcc
	ds_read2_b32 v[64:65], v169 offset0:30 offset1:31
	v_cndmask_b32_e32 v0, v0, v63, vcc
	s_waitcnt lgkmcnt(0)
	v_cmp_gt_f32_e32 vcc, v64, v0
	s_nop 1
	v_cndmask_b32_e32 v0, v0, v64, vcc
	v_cndmask_b32_e64 v72, v72, 30, vcc
	v_cmp_gt_f32_e32 vcc, v65, v0
	s_nop 1
	v_cndmask_b32_e64 v72, v72, 31, vcc
	v_cndmask_b32_e32 v80, v0, v65, vcc
	v_cmp_ne_u32_e64 s[0:1], 0, v72
	v_cmp_lg_f32_e32 vcc, s64, v2
	v_lshlrev_b32_e64 v0, v72, 1
	s_and_b64 s[0:1], s[0:1], vcc
	v_cndmask_b32_e64 v81, v171, v2, s[0:1]
	v_and_b32_e32 v82, 2, v0
	v_cmp_eq_u32_e64 s[0:1], 0, v82
	v_cmp_gt_f32_e64 s[6:7], v3, v81
	s_and_b64 s[0:1], s[0:1], s[6:7]
	v_cndmask_b32_e64 v81, v81, v3, s[0:1]
	v_and_b32_e32 v83, 4, v0
	v_cndmask_b32_e64 v82, 0, 1, s[0:1]
	v_cmp_eq_u32_e64 s[0:1], 0, v83
	v_cmp_gt_f32_e64 s[6:7], v4, v81
	s_and_b64 s[0:1], s[0:1], s[6:7]
	v_cndmask_b32_e64 v81, v81, v4, s[0:1]
	v_and_b32_e32 v83, 8, v0
	v_cndmask_b32_e64 v82, v82, 2, s[0:1]
	v_cmp_eq_u32_e64 s[0:1], 0, v83
	v_cmp_gt_f32_e64 s[6:7], v5, v81
	s_and_b64 s[0:1], s[0:1], s[6:7]
	v_cndmask_b32_e64 v81, v81, v5, s[0:1]
	v_and_b32_e32 v83, 16, v0
	v_cndmask_b32_e64 v82, v82, 3, s[0:1]
	v_cmp_eq_u32_e64 s[0:1], 0, v83
	v_cmp_gt_f32_e64 s[6:7], v6, v81
	s_and_b64 s[0:1], s[0:1], s[6:7]
	v_cndmask_b32_e64 v81, v81, v6, s[0:1]
	v_and_b32_e32 v83, 32, v0
	v_cndmask_b32_e64 v82, v82, 4, s[0:1]
	v_cmp_eq_u32_e64 s[0:1], 0, v83
	v_cmp_gt_f32_e64 s[6:7], v7, v81
	s_and_b64 s[0:1], s[0:1], s[6:7]
	v_cndmask_b32_e64 v81, v81, v7, s[0:1]
	v_and_b32_e32 v83, 64, v0
	v_cndmask_b32_e64 v82, v82, 5, s[0:1]
	v_cmp_eq_u32_e64 s[0:1], 0, v83
	v_cmp_gt_f32_e64 s[6:7], v8, v81
	s_and_b64 s[0:1], s[0:1], s[6:7]
	v_cndmask_b32_e64 v81, v81, v8, s[0:1]
	v_and_b32_e32 v83, 0x80, v0
	v_cndmask_b32_e64 v82, v82, 6, s[0:1]
	v_cmp_eq_u32_e64 s[0:1], 0, v83
	v_cmp_gt_f32_e64 s[6:7], v9, v81
	s_and_b64 s[0:1], s[0:1], s[6:7]
	v_cndmask_b32_e64 v81, v81, v9, s[0:1]
	v_and_b32_e32 v83, 0x100, v0
	v_cndmask_b32_e64 v82, v82, 7, s[0:1]
	v_cmp_eq_u32_e64 s[0:1], 0, v83
	v_cmp_gt_f32_e64 s[6:7], v10, v81
	s_and_b64 s[0:1], s[0:1], s[6:7]
	v_cndmask_b32_e64 v81, v81, v10, s[0:1]
	v_and_b32_e32 v83, 0x200, v0
	v_cndmask_b32_e64 v82, v82, 8, s[0:1]
	v_cmp_eq_u32_e64 s[0:1], 0, v83
	v_cmp_gt_f32_e64 s[6:7], v11, v81
	s_and_b64 s[0:1], s[0:1], s[6:7]
	v_cndmask_b32_e64 v81, v81, v11, s[0:1]
	v_and_b32_e32 v83, 0x400, v0
	v_cndmask_b32_e64 v82, v82, 9, s[0:1]
	v_cmp_eq_u32_e64 s[0:1], 0, v83
	v_cmp_gt_f32_e64 s[6:7], v12, v81
	s_and_b64 s[0:1], s[0:1], s[6:7]
	v_cndmask_b32_e64 v81, v81, v12, s[0:1]
	v_and_b32_e32 v83, 0x800, v0
	v_cndmask_b32_e64 v82, v82, 10, s[0:1]
	v_cmp_eq_u32_e64 s[0:1], 0, v83
	v_cmp_gt_f32_e64 s[6:7], v13, v81
	s_and_b64 s[0:1], s[0:1], s[6:7]
	v_cndmask_b32_e64 v81, v81, v13, s[0:1]
	v_and_b32_e32 v83, 0x1000, v0
	v_cndmask_b32_e64 v82, v82, 11, s[0:1]
	v_cmp_eq_u32_e64 s[0:1], 0, v83
	v_cmp_gt_f32_e64 s[6:7], v14, v81
	s_and_b64 s[0:1], s[0:1], s[6:7]
	v_cndmask_b32_e64 v81, v81, v14, s[0:1]
	v_and_b32_e32 v83, 0x2000, v0
	v_cndmask_b32_e64 v82, v82, 12, s[0:1]
	v_cmp_eq_u32_e64 s[0:1], 0, v83
	v_cmp_gt_f32_e64 s[6:7], v15, v81
	s_and_b64 s[0:1], s[0:1], s[6:7]
	v_cndmask_b32_e64 v81, v81, v15, s[0:1]
	v_and_b32_e32 v83, 0x4000, v0
	v_cndmask_b32_e64 v82, v82, 13, s[0:1]
	v_cmp_eq_u32_e64 s[0:1], 0, v83
	v_cmp_gt_f32_e64 s[6:7], v16, v81
	s_and_b64 s[0:1], s[0:1], s[6:7]
	v_cndmask_b32_e64 v81, v81, v16, s[0:1]
	v_and_b32_e32 v83, 0x8000, v0
	v_cndmask_b32_e64 v82, v82, 14, s[0:1]
	v_cmp_eq_u32_e64 s[0:1], 0, v83
	v_cmp_gt_f32_e64 s[6:7], v17, v81
	s_and_b64 s[0:1], s[0:1], s[6:7]
	v_cndmask_b32_e64 v81, v81, v17, s[0:1]
	v_and_b32_e32 v83, 0x10000, v0
	v_cndmask_b32_e64 v82, v82, 15, s[0:1]
	v_cmp_eq_u32_e64 s[0:1], 0, v83
	v_cmp_gt_f32_e64 s[6:7], v50, v81
	s_and_b64 s[0:1], s[0:1], s[6:7]
	v_cndmask_b32_e64 v81, v81, v50, s[0:1]
	v_and_b32_e32 v83, 0x20000, v0
	v_cndmask_b32_e64 v82, v82, 16, s[0:1]
	v_cmp_eq_u32_e64 s[0:1], 0, v83
	v_cmp_gt_f32_e64 s[6:7], v51, v81
	s_and_b64 s[0:1], s[0:1], s[6:7]
	v_cndmask_b32_e64 v81, v81, v51, s[0:1]
	v_and_b32_e32 v83, 0x40000, v0
	v_cndmask_b32_e64 v82, v82, 17, s[0:1]
	v_cmp_eq_u32_e64 s[0:1], 0, v83
	v_cmp_gt_f32_e64 s[6:7], v52, v81
	s_and_b64 s[0:1], s[0:1], s[6:7]
	v_cndmask_b32_e64 v81, v81, v52, s[0:1]
	v_and_b32_e32 v83, 0x80000, v0
	v_cndmask_b32_e64 v82, v82, 18, s[0:1]
	v_cmp_eq_u32_e64 s[0:1], 0, v83
	v_cmp_gt_f32_e64 s[6:7], v53, v81
	s_and_b64 s[0:1], s[0:1], s[6:7]
	v_cndmask_b32_e64 v81, v81, v53, s[0:1]
	v_and_b32_e32 v83, 0x100000, v0
	v_cndmask_b32_e64 v82, v82, 19, s[0:1]
	v_cmp_eq_u32_e64 s[0:1], 0, v83
	v_cmp_gt_f32_e64 s[6:7], v54, v81
	s_and_b64 s[0:1], s[0:1], s[6:7]
	v_cndmask_b32_e64 v81, v81, v54, s[0:1]
	v_and_b32_e32 v83, 0x200000, v0
	v_cndmask_b32_e64 v82, v82, 20, s[0:1]
	v_cmp_eq_u32_e64 s[0:1], 0, v83
	v_cmp_gt_f32_e64 s[6:7], v55, v81
	s_and_b64 s[0:1], s[0:1], s[6:7]
	v_cndmask_b32_e64 v81, v81, v55, s[0:1]
	v_and_b32_e32 v83, 0x400000, v0
	v_cndmask_b32_e64 v82, v82, 21, s[0:1]
	v_cmp_eq_u32_e64 s[0:1], 0, v83
	v_cmp_gt_f32_e64 s[6:7], v56, v81
	s_and_b64 s[0:1], s[0:1], s[6:7]
	v_cndmask_b32_e64 v81, v81, v56, s[0:1]
	v_and_b32_e32 v83, 0x800000, v0
	v_cndmask_b32_e64 v82, v82, 22, s[0:1]
	v_cmp_eq_u32_e64 s[0:1], 0, v83
	v_cmp_gt_f32_e64 s[6:7], v57, v81
	s_and_b64 s[0:1], s[0:1], s[6:7]
	v_cndmask_b32_e64 v81, v81, v57, s[0:1]
	v_and_b32_e32 v83, 0x1000000, v0
	v_cndmask_b32_e64 v82, v82, 23, s[0:1]
	v_cmp_eq_u32_e64 s[0:1], 0, v83
	v_cmp_gt_f32_e64 s[6:7], v58, v81
	s_and_b64 s[0:1], s[0:1], s[6:7]
	v_cndmask_b32_e64 v81, v81, v58, s[0:1]
	v_and_b32_e32 v83, 0x2000000, v0
	v_cndmask_b32_e64 v82, v82, 24, s[0:1]
	v_cmp_eq_u32_e64 s[0:1], 0, v83
	v_cmp_gt_f32_e64 s[6:7], v59, v81
	s_and_b64 s[0:1], s[0:1], s[6:7]
	v_cndmask_b32_e64 v81, v81, v59, s[0:1]
	v_and_b32_e32 v83, 0x4000000, v0
	v_cndmask_b32_e64 v82, v82, 25, s[0:1]
	v_cmp_eq_u32_e64 s[0:1], 0, v83
	v_cmp_gt_f32_e64 s[6:7], v60, v81
	s_and_b64 s[0:1], s[0:1], s[6:7]
	v_cndmask_b32_e64 v81, v81, v60, s[0:1]
	v_and_b32_e32 v83, 0x8000000, v0
	v_cndmask_b32_e64 v82, v82, 26, s[0:1]
	v_cmp_eq_u32_e64 s[0:1], 0, v83
	v_cmp_gt_f32_e64 s[6:7], v61, v81
	s_and_b64 s[0:1], s[0:1], s[6:7]
	v_cndmask_b32_e64 v81, v81, v61, s[0:1]
	v_and_b32_e32 v83, 0x10000000, v0
	v_cndmask_b32_e64 v82, v82, 27, s[0:1]
	v_cmp_eq_u32_e64 s[0:1], 0, v83
	v_cmp_gt_f32_e64 s[6:7], v62, v81
	s_and_b64 s[0:1], s[0:1], s[6:7]
	v_cndmask_b32_e64 v81, v81, v62, s[0:1]
	v_and_b32_e32 v83, 0x20000000, v0
	v_cndmask_b32_e64 v82, v82, 28, s[0:1]
	v_cmp_eq_u32_e64 s[0:1], 0, v83
	v_cmp_gt_f32_e64 s[6:7], v63, v81
	s_and_b64 s[0:1], s[0:1], s[6:7]
	v_cndmask_b32_e64 v81, v81, v63, s[0:1]
	v_and_b32_e32 v83, 2.0, v0
	v_cndmask_b32_e64 v82, v82, 29, s[0:1]
	v_cmp_eq_u32_e64 s[0:1], 0, v83
	v_cmp_gt_f32_e64 s[6:7], v64, v81
	s_and_b64 s[0:1], s[0:1], s[6:7]
	v_cndmask_b32_e64 v81, v81, v64, s[0:1]
	v_cndmask_b32_e64 v82, v82, 30, s[0:1]
	v_cmp_ne_u32_e64 s[0:1], 31, v72
	v_cmp_gt_f32_e64 s[6:7], v65, v81
	s_and_b64 s[0:1], s[0:1], s[6:7]
	v_cndmask_b32_e64 v82, v82, 31, s[0:1]
	v_lshlrev_b32_e64 v83, v82, 1
	v_bitop3_b32 v85, v83, 1, v0 bitop3:0xc8
	v_cndmask_b32_e64 v81, v81, v65, s[0:1]
	v_cmp_eq_u32_e64 s[0:1], 0, v85
	s_and_b64 s[0:1], s[0:1], vcc
	v_bitop3_b32 v86, v83, 2, v0 bitop3:0xc8
	v_cndmask_b32_e64 v85, v171, v2, s[0:1]
	v_cmp_eq_u32_e64 s[0:1], 0, v86
	v_cmp_gt_f32_e64 s[6:7], v3, v85
	s_and_b64 s[0:1], s[0:1], s[6:7]
	v_cndmask_b32_e64 v85, v85, v3, s[0:1]
	v_bitop3_b32 v87, v83, 4, v0 bitop3:0xc8
	v_cndmask_b32_e64 v86, 0, 1, s[0:1]
	v_cmp_eq_u32_e64 s[0:1], 0, v87
	v_cmp_gt_f32_e64 s[6:7], v4, v85
	s_and_b64 s[0:1], s[0:1], s[6:7]
	v_cndmask_b32_e64 v85, v85, v4, s[0:1]
	v_bitop3_b32 v87, v83, 8, v0 bitop3:0xc8
	v_cndmask_b32_e64 v86, v86, 2, s[0:1]
	v_cmp_eq_u32_e64 s[0:1], 0, v87
	v_cmp_gt_f32_e64 s[6:7], v5, v85
	s_and_b64 s[0:1], s[0:1], s[6:7]
	v_cndmask_b32_e64 v85, v85, v5, s[0:1]
	v_bitop3_b32 v87, v83, 16, v0 bitop3:0xc8
	v_cndmask_b32_e64 v86, v86, 3, s[0:1]
	v_cmp_eq_u32_e64 s[0:1], 0, v87
	v_cmp_gt_f32_e64 s[6:7], v6, v85
	s_and_b64 s[0:1], s[0:1], s[6:7]
	v_cndmask_b32_e64 v85, v85, v6, s[0:1]
	v_bitop3_b32 v87, v83, 32, v0 bitop3:0xc8
	v_cndmask_b32_e64 v86, v86, 4, s[0:1]
	v_cmp_eq_u32_e64 s[0:1], 0, v87
	v_cmp_gt_f32_e64 s[6:7], v7, v85
	s_and_b64 s[0:1], s[0:1], s[6:7]
	v_cndmask_b32_e64 v85, v85, v7, s[0:1]
	v_bitop3_b32 v87, v83, 64, v0 bitop3:0xc8
	v_cndmask_b32_e64 v86, v86, 5, s[0:1]
	v_cmp_eq_u32_e64 s[0:1], 0, v87
	v_cmp_gt_f32_e64 s[6:7], v8, v85
	s_and_b64 s[0:1], s[0:1], s[6:7]
	v_cndmask_b32_e64 v85, v85, v8, s[0:1]
	v_bitop3_b32 v87, v83, s65, v0 bitop3:0xc8
	v_cndmask_b32_e64 v86, v86, 6, s[0:1]
	v_cmp_eq_u32_e64 s[0:1], 0, v87
	v_cmp_gt_f32_e64 s[6:7], v9, v85
	s_and_b64 s[0:1], s[0:1], s[6:7]
	v_cndmask_b32_e64 v85, v85, v9, s[0:1]
	v_bitop3_b32 v87, v83, s66, v0 bitop3:0xc8
	v_cndmask_b32_e64 v86, v86, 7, s[0:1]
	v_cmp_eq_u32_e64 s[0:1], 0, v87
	v_cmp_gt_f32_e64 s[6:7], v10, v85
	s_and_b64 s[0:1], s[0:1], s[6:7]
	v_cndmask_b32_e64 v85, v85, v10, s[0:1]
	v_bitop3_b32 v87, v83, s67, v0 bitop3:0xc8
	v_cndmask_b32_e64 v86, v86, 8, s[0:1]
	v_cmp_eq_u32_e64 s[0:1], 0, v87
	v_cmp_gt_f32_e64 s[6:7], v11, v85
	s_and_b64 s[0:1], s[0:1], s[6:7]
	v_cndmask_b32_e64 v85, v85, v11, s[0:1]
	v_bitop3_b32 v87, v83, s48, v0 bitop3:0xc8
	v_cndmask_b32_e64 v86, v86, 9, s[0:1]
	v_cmp_eq_u32_e64 s[0:1], 0, v87
	v_cmp_gt_f32_e64 s[6:7], v12, v85
	s_and_b64 s[0:1], s[0:1], s[6:7]
	v_cndmask_b32_e64 v85, v85, v12, s[0:1]
	v_bitop3_b32 v87, v83, s69, v0 bitop3:0xc8
	v_cndmask_b32_e64 v86, v86, 10, s[0:1]
	v_cmp_eq_u32_e64 s[0:1], 0, v87
	v_cmp_gt_f32_e64 s[6:7], v13, v85
	s_and_b64 s[0:1], s[0:1], s[6:7]
	v_cndmask_b32_e64 v85, v85, v13, s[0:1]
	v_bitop3_b32 v87, v83, s19, v0 bitop3:0xc8
	v_cndmask_b32_e64 v86, v86, 11, s[0:1]
	v_cmp_eq_u32_e64 s[0:1], 0, v87
	v_cmp_gt_f32_e64 s[6:7], v14, v85
	s_and_b64 s[0:1], s[0:1], s[6:7]
	v_cndmask_b32_e64 v85, v85, v14, s[0:1]
	v_bitop3_b32 v87, v83, s61, v0 bitop3:0xc8
	v_cndmask_b32_e64 v86, v86, 12, s[0:1]
	v_cmp_eq_u32_e64 s[0:1], 0, v87
	v_cmp_gt_f32_e64 s[6:7], v15, v85
	s_and_b64 s[0:1], s[0:1], s[6:7]
	v_cndmask_b32_e64 v85, v85, v15, s[0:1]
	v_bitop3_b32 v87, v83, s63, v0 bitop3:0xc8
	v_cndmask_b32_e64 v86, v86, 13, s[0:1]
	v_cmp_eq_u32_e64 s[0:1], 0, v87
	v_cmp_gt_f32_e64 s[6:7], v16, v85
	s_and_b64 s[0:1], s[0:1], s[6:7]
	v_cndmask_b32_e64 v85, v85, v16, s[0:1]
	v_bitop3_b32 v87, v83, s53, v0 bitop3:0xc8
	v_cndmask_b32_e64 v86, v86, 14, s[0:1]
	v_cmp_eq_u32_e64 s[0:1], 0, v87
	v_cmp_gt_f32_e64 s[6:7], v17, v85
	s_and_b64 s[0:1], s[0:1], s[6:7]
	v_cndmask_b32_e64 v85, v85, v17, s[0:1]
	v_bitop3_b32 v87, v83, s54, v0 bitop3:0xc8
	v_cndmask_b32_e64 v86, v86, 15, s[0:1]
	v_cmp_eq_u32_e64 s[0:1], 0, v87
	v_cmp_gt_f32_e64 s[6:7], v50, v85
	s_and_b64 s[0:1], s[0:1], s[6:7]
	v_cndmask_b32_e64 v85, v85, v50, s[0:1]
	v_bitop3_b32 v87, v83, s70, v0 bitop3:0xc8
	v_cndmask_b32_e64 v86, v86, 16, s[0:1]
	v_cmp_eq_u32_e64 s[0:1], 0, v87
	v_cmp_gt_f32_e64 s[6:7], v51, v85
	s_and_b64 s[0:1], s[0:1], s[6:7]
	v_cndmask_b32_e64 v85, v85, v51, s[0:1]
	v_bitop3_b32 v87, v83, s71, v0 bitop3:0xc8
	v_cndmask_b32_e64 v86, v86, 17, s[0:1]
	v_cmp_eq_u32_e64 s[0:1], 0, v87
	v_cmp_gt_f32_e64 s[6:7], v52, v85
	s_and_b64 s[0:1], s[0:1], s[6:7]
	v_cndmask_b32_e64 v85, v85, v52, s[0:1]
	v_bitop3_b32 v87, v83, s73, v0 bitop3:0xc8
	v_cndmask_b32_e64 v86, v86, 18, s[0:1]
	v_cmp_eq_u32_e64 s[0:1], 0, v87
	v_cmp_gt_f32_e64 s[6:7], v53, v85
	s_and_b64 s[0:1], s[0:1], s[6:7]
	v_cndmask_b32_e64 v85, v85, v53, s[0:1]
	v_bitop3_b32 v87, v83, s75, v0 bitop3:0xc8
	v_cndmask_b32_e64 v86, v86, 19, s[0:1]
	v_cmp_eq_u32_e64 s[0:1], 0, v87
	v_cmp_gt_f32_e64 s[6:7], v54, v85
	s_and_b64 s[0:1], s[0:1], s[6:7]
	v_cndmask_b32_e64 v85, v85, v54, s[0:1]
	v_bitop3_b32 v87, v83, s76, v0 bitop3:0xc8
	v_cndmask_b32_e64 v86, v86, 20, s[0:1]
	v_cmp_eq_u32_e64 s[0:1], 0, v87
	v_cmp_gt_f32_e64 s[6:7], v55, v85
	s_and_b64 s[0:1], s[0:1], s[6:7]
	v_cndmask_b32_e64 v85, v85, v55, s[0:1]
	v_bitop3_b32 v87, v83, s77, v0 bitop3:0xc8
	v_cndmask_b32_e64 v86, v86, 21, s[0:1]
	v_cmp_eq_u32_e64 s[0:1], 0, v87
	v_cmp_gt_f32_e64 s[6:7], v56, v85
	s_and_b64 s[0:1], s[0:1], s[6:7]
	v_cndmask_b32_e64 v85, v85, v56, s[0:1]
	v_bitop3_b32 v87, v83, s62, v0 bitop3:0xc8
	v_cndmask_b32_e64 v86, v86, 22, s[0:1]
	v_cmp_eq_u32_e64 s[0:1], 0, v87
	v_cmp_gt_f32_e64 s[6:7], v57, v85
	s_and_b64 s[0:1], s[0:1], s[6:7]
	v_cndmask_b32_e64 v85, v85, v57, s[0:1]
	v_bitop3_b32 v87, v83, s78, v0 bitop3:0xc8
	v_cndmask_b32_e64 v86, v86, 23, s[0:1]
	v_cmp_eq_u32_e64 s[0:1], 0, v87
	v_cmp_gt_f32_e64 s[6:7], v58, v85
	s_and_b64 s[0:1], s[0:1], s[6:7]
	v_cndmask_b32_e64 v85, v85, v58, s[0:1]
	v_bitop3_b32 v87, v83, s79, v0 bitop3:0xc8
	v_cndmask_b32_e64 v86, v86, 24, s[0:1]
	v_cmp_eq_u32_e64 s[0:1], 0, v87
	v_cmp_gt_f32_e64 s[6:7], v59, v85
	s_and_b64 s[0:1], s[0:1], s[6:7]
	v_cndmask_b32_e64 v85, v85, v59, s[0:1]
	v_bitop3_b32 v87, v83, s80, v0 bitop3:0xc8
	v_cndmask_b32_e64 v86, v86, 25, s[0:1]
	v_cmp_eq_u32_e64 s[0:1], 0, v87
	v_cmp_gt_f32_e64 s[6:7], v60, v85
	s_and_b64 s[0:1], s[0:1], s[6:7]
	v_cndmask_b32_e64 v85, v85, v60, s[0:1]
	v_bitop3_b32 v87, v83, s81, v0 bitop3:0xc8
	v_cndmask_b32_e64 v86, v86, 26, s[0:1]
	v_cmp_eq_u32_e64 s[0:1], 0, v87
	v_cmp_gt_f32_e64 s[6:7], v61, v85
	s_and_b64 s[0:1], s[0:1], s[6:7]
	v_cndmask_b32_e64 v85, v85, v61, s[0:1]
	v_bitop3_b32 v87, v83, s82, v0 bitop3:0xc8
	v_cndmask_b32_e64 v86, v86, 27, s[0:1]
	v_cmp_eq_u32_e64 s[0:1], 0, v87
	v_cmp_gt_f32_e64 s[6:7], v62, v85
	s_and_b64 s[0:1], s[0:1], s[6:7]
	v_cndmask_b32_e64 v85, v85, v62, s[0:1]
	v_bitop3_b32 v87, v83, s83, v0 bitop3:0xc8
	v_cndmask_b32_e64 v86, v86, 28, s[0:1]
	v_cmp_eq_u32_e64 s[0:1], 0, v87
	v_cmp_gt_f32_e64 s[6:7], v63, v85
	s_and_b64 s[0:1], s[0:1], s[6:7]
	v_or_b32_e32 v84, v83, v0
	v_cndmask_b32_e64 v85, v85, v63, s[0:1]
	v_bitop3_b32 v0, v83, 2.0, v0 bitop3:0xc8
	v_cndmask_b32_e64 v86, v86, 29, s[0:1]
	v_cmp_eq_u32_e64 s[0:1], 0, v0
	v_cmp_gt_f32_e64 s[6:7], v64, v85
	s_and_b64 s[0:1], s[0:1], s[6:7]
	v_cndmask_b32_e64 v0, v85, v64, s[0:1]
	v_cndmask_b32_e64 v83, v86, 30, s[0:1]
	v_cmp_lt_i32_e64 s[0:1], -1, v84
	v_cmp_gt_f32_e64 s[6:7], v65, v0
	s_and_b64 s[0:1], s[0:1], s[6:7]
	v_cndmask_b32_e64 v83, v83, 31, s[0:1]
	v_lshlrev_b32_e64 v85, v83, 1
	v_bitop3_b32 v87, v85, 1, v84 bitop3:0xc8
	v_cndmask_b32_e64 v0, v0, v65, s[0:1]
	v_cmp_eq_u32_e64 s[0:1], 0, v87
	s_and_b64 vcc, s[0:1], vcc
	v_cndmask_b32_e32 v2, v171, v2, vcc
	v_bitop3_b32 v87, v85, 2, v84 bitop3:0xc8
	v_cmp_eq_u32_e32 vcc, 0, v87
	v_cmp_gt_f32_e64 s[0:1], v3, v2
	s_and_b64 vcc, vcc, s[0:1]
	v_cndmask_b32_e32 v2, v2, v3, vcc
	v_bitop3_b32 v87, v85, 4, v84 bitop3:0xc8
	v_cndmask_b32_e64 v3, 0, 1, vcc
	v_cmp_eq_u32_e32 vcc, 0, v87
	v_cmp_gt_f32_e64 s[0:1], v4, v2
	s_and_b64 vcc, vcc, s[0:1]
	v_cndmask_b32_e32 v2, v2, v4, vcc
	v_bitop3_b32 v4, v85, 8, v84 bitop3:0xc8
	v_cndmask_b32_e64 v3, v3, 2, vcc
	v_cmp_eq_u32_e32 vcc, 0, v4
	v_cmp_gt_f32_e64 s[0:1], v5, v2
	s_and_b64 vcc, vcc, s[0:1]
	v_cndmask_b32_e32 v2, v2, v5, vcc
	v_bitop3_b32 v4, v85, 16, v84 bitop3:0xc8
	v_cndmask_b32_e64 v3, v3, 3, vcc
	v_cmp_eq_u32_e32 vcc, 0, v4
	v_cmp_gt_f32_e64 s[0:1], v6, v2
	s_and_b64 vcc, vcc, s[0:1]
	v_cndmask_b32_e32 v2, v2, v6, vcc
	v_bitop3_b32 v4, v85, 32, v84 bitop3:0xc8
	v_cndmask_b32_e64 v3, v3, 4, vcc
	v_cmp_eq_u32_e32 vcc, 0, v4
	v_cmp_gt_f32_e64 s[0:1], v7, v2
	s_and_b64 vcc, vcc, s[0:1]
	v_cndmask_b32_e32 v2, v2, v7, vcc
	v_bitop3_b32 v4, v85, 64, v84 bitop3:0xc8
	v_cndmask_b32_e64 v3, v3, 5, vcc
	v_cmp_eq_u32_e32 vcc, 0, v4
	v_cmp_gt_f32_e64 s[0:1], v8, v2
	s_and_b64 vcc, vcc, s[0:1]
	v_cndmask_b32_e32 v2, v2, v8, vcc
	v_bitop3_b32 v4, v85, s65, v84 bitop3:0xc8
	v_cndmask_b32_e64 v3, v3, 6, vcc
	v_cmp_eq_u32_e32 vcc, 0, v4
	v_cmp_gt_f32_e64 s[0:1], v9, v2
	s_and_b64 vcc, vcc, s[0:1]
	v_cndmask_b32_e32 v2, v2, v9, vcc
	v_bitop3_b32 v4, v85, s66, v84 bitop3:0xc8
	v_cndmask_b32_e64 v3, v3, 7, vcc
	v_cmp_eq_u32_e32 vcc, 0, v4
	v_cmp_gt_f32_e64 s[0:1], v10, v2
	s_and_b64 vcc, vcc, s[0:1]
	v_cndmask_b32_e32 v2, v2, v10, vcc
	v_bitop3_b32 v4, v85, s67, v84 bitop3:0xc8
	v_cndmask_b32_e64 v3, v3, 8, vcc
	v_cmp_eq_u32_e32 vcc, 0, v4
	v_cmp_gt_f32_e64 s[0:1], v11, v2
	s_and_b64 vcc, vcc, s[0:1]
	v_cndmask_b32_e32 v2, v2, v11, vcc
	v_bitop3_b32 v4, v85, s48, v84 bitop3:0xc8
	v_cndmask_b32_e64 v3, v3, 9, vcc
	v_cmp_eq_u32_e32 vcc, 0, v4
	v_cmp_gt_f32_e64 s[0:1], v12, v2
	s_and_b64 vcc, vcc, s[0:1]
	v_cndmask_b32_e32 v2, v2, v12, vcc
	v_bitop3_b32 v4, v85, s69, v84 bitop3:0xc8
	v_cndmask_b32_e64 v3, v3, 10, vcc
	v_cmp_eq_u32_e32 vcc, 0, v4
	v_cmp_gt_f32_e64 s[0:1], v13, v2
	s_and_b64 vcc, vcc, s[0:1]
	v_cndmask_b32_e32 v2, v2, v13, vcc
	v_bitop3_b32 v4, v85, s19, v84 bitop3:0xc8
	v_cndmask_b32_e64 v3, v3, 11, vcc
	v_cmp_eq_u32_e32 vcc, 0, v4
	v_cmp_gt_f32_e64 s[0:1], v14, v2
	s_and_b64 vcc, vcc, s[0:1]
	v_cndmask_b32_e32 v2, v2, v14, vcc
	v_bitop3_b32 v4, v85, s61, v84 bitop3:0xc8
	v_cndmask_b32_e64 v3, v3, 12, vcc
	v_cmp_eq_u32_e32 vcc, 0, v4
	v_cmp_gt_f32_e64 s[0:1], v15, v2
	s_and_b64 vcc, vcc, s[0:1]
	v_cndmask_b32_e32 v2, v2, v15, vcc
	v_bitop3_b32 v4, v85, s63, v84 bitop3:0xc8
	v_cndmask_b32_e64 v3, v3, 13, vcc
	v_cmp_eq_u32_e32 vcc, 0, v4
	v_cmp_gt_f32_e64 s[0:1], v16, v2
	s_and_b64 vcc, vcc, s[0:1]
	v_cndmask_b32_e32 v2, v2, v16, vcc
	v_bitop3_b32 v4, v85, s53, v84 bitop3:0xc8
	v_cndmask_b32_e64 v3, v3, 14, vcc
	v_cmp_eq_u32_e32 vcc, 0, v4
	v_cmp_gt_f32_e64 s[0:1], v17, v2
	s_and_b64 vcc, vcc, s[0:1]
	v_cndmask_b32_e32 v2, v2, v17, vcc
	v_bitop3_b32 v4, v85, s54, v84 bitop3:0xc8
	v_cndmask_b32_e64 v3, v3, 15, vcc
	v_cmp_eq_u32_e32 vcc, 0, v4
	v_cmp_gt_f32_e64 s[0:1], v50, v2
	s_and_b64 vcc, vcc, s[0:1]
	v_cndmask_b32_e32 v2, v2, v50, vcc
	v_bitop3_b32 v4, v85, s70, v84 bitop3:0xc8
	v_cndmask_b32_e64 v3, v3, 16, vcc
	v_cmp_eq_u32_e32 vcc, 0, v4
	v_cmp_gt_f32_e64 s[0:1], v51, v2
	s_and_b64 vcc, vcc, s[0:1]
	v_cndmask_b32_e32 v2, v2, v51, vcc
	v_bitop3_b32 v4, v85, s71, v84 bitop3:0xc8
	v_cndmask_b32_e64 v3, v3, 17, vcc
	v_cmp_eq_u32_e32 vcc, 0, v4
	v_cmp_gt_f32_e64 s[0:1], v52, v2
	s_and_b64 vcc, vcc, s[0:1]
	v_cndmask_b32_e32 v2, v2, v52, vcc
	v_bitop3_b32 v4, v85, s73, v84 bitop3:0xc8
	v_cndmask_b32_e64 v3, v3, 18, vcc
	v_cmp_eq_u32_e32 vcc, 0, v4
	v_cmp_gt_f32_e64 s[0:1], v53, v2
	s_and_b64 vcc, vcc, s[0:1]
	v_cndmask_b32_e32 v2, v2, v53, vcc
	v_bitop3_b32 v4, v85, s75, v84 bitop3:0xc8
	v_cndmask_b32_e64 v3, v3, 19, vcc
	v_cmp_eq_u32_e32 vcc, 0, v4
	v_cmp_gt_f32_e64 s[0:1], v54, v2
	s_and_b64 vcc, vcc, s[0:1]
	v_cndmask_b32_e32 v2, v2, v54, vcc
	v_bitop3_b32 v4, v85, s76, v84 bitop3:0xc8
	v_cndmask_b32_e64 v3, v3, 20, vcc
	v_cmp_eq_u32_e32 vcc, 0, v4
	v_cmp_gt_f32_e64 s[0:1], v55, v2
	s_and_b64 vcc, vcc, s[0:1]
	v_cndmask_b32_e32 v2, v2, v55, vcc
	v_bitop3_b32 v4, v85, s77, v84 bitop3:0xc8
	v_cndmask_b32_e64 v3, v3, 21, vcc
	v_cmp_eq_u32_e32 vcc, 0, v4
	v_cmp_gt_f32_e64 s[0:1], v56, v2
	s_and_b64 vcc, vcc, s[0:1]
	v_cndmask_b32_e32 v2, v2, v56, vcc
	v_bitop3_b32 v4, v85, s62, v84 bitop3:0xc8
	v_cndmask_b32_e64 v3, v3, 22, vcc
	v_cmp_eq_u32_e32 vcc, 0, v4
	v_cmp_gt_f32_e64 s[0:1], v57, v2
	s_and_b64 vcc, vcc, s[0:1]
	v_cndmask_b32_e32 v2, v2, v57, vcc
	v_bitop3_b32 v4, v85, s78, v84 bitop3:0xc8
	v_cndmask_b32_e64 v3, v3, 23, vcc
	v_cmp_eq_u32_e32 vcc, 0, v4
	v_cmp_gt_f32_e64 s[0:1], v58, v2
	s_and_b64 vcc, vcc, s[0:1]
	v_cndmask_b32_e32 v2, v2, v58, vcc
	v_bitop3_b32 v4, v85, s79, v84 bitop3:0xc8
	v_cndmask_b32_e64 v3, v3, 24, vcc
	v_cmp_eq_u32_e32 vcc, 0, v4
	v_cmp_gt_f32_e64 s[0:1], v59, v2
	s_and_b64 vcc, vcc, s[0:1]
	v_cndmask_b32_e32 v2, v2, v59, vcc
	v_bitop3_b32 v4, v85, s80, v84 bitop3:0xc8
	v_cndmask_b32_e64 v3, v3, 25, vcc
	v_cmp_eq_u32_e32 vcc, 0, v4
	v_cmp_gt_f32_e64 s[0:1], v60, v2
	s_and_b64 vcc, vcc, s[0:1]
	v_cndmask_b32_e32 v2, v2, v60, vcc
	v_bitop3_b32 v4, v85, s81, v84 bitop3:0xc8
	v_cndmask_b32_e64 v3, v3, 26, vcc
	v_cmp_eq_u32_e32 vcc, 0, v4
	v_cmp_gt_f32_e64 s[0:1], v61, v2
	s_and_b64 vcc, vcc, s[0:1]
	v_cndmask_b32_e32 v2, v2, v61, vcc
	v_bitop3_b32 v4, v85, s82, v84 bitop3:0xc8
	v_cndmask_b32_e64 v3, v3, 27, vcc
	v_cmp_eq_u32_e32 vcc, 0, v4
	v_cmp_gt_f32_e64 s[0:1], v62, v2
	s_and_b64 vcc, vcc, s[0:1]
	v_cndmask_b32_e32 v2, v2, v62, vcc
	v_bitop3_b32 v4, v85, s83, v84 bitop3:0xc8
	v_cndmask_b32_e64 v3, v3, 28, vcc
	v_cmp_eq_u32_e32 vcc, 0, v4
	v_cmp_gt_f32_e64 s[0:1], v63, v2
	s_and_b64 vcc, vcc, s[0:1]
	v_cndmask_b32_e32 v2, v2, v63, vcc
	v_bitop3_b32 v4, v85, 2.0, v84 bitop3:0xc8
	v_cndmask_b32_e64 v3, v3, 29, vcc
	v_cmp_eq_u32_e32 vcc, 0, v4
	v_cmp_gt_f32_e64 s[0:1], v64, v2
	s_and_b64 vcc, vcc, s[0:1]
	v_or_b32_e32 v86, v85, v84
	v_cndmask_b32_e32 v2, v2, v64, vcc
	v_cndmask_b32_e64 v3, v3, 30, vcc
	v_cmp_lt_i32_e32 vcc, -1, v86
	v_cmp_gt_f32_e64 s[0:1], v65, v2
	s_and_b64 vcc, vcc, s[0:1]
	v_cndmask_b32_e32 v5, v2, v65, vcc
	v_sub_f32_e32 v2, v80, v80
	v_cndmask_b32_e64 v8, v3, 31, vcc
	v_mul_f32_e32 v2, 0x3fb8aa3b, v2
	v_sub_f32_e32 v3, v81, v80
	v_exp_f32_e32 v2, v2
	v_mul_f32_e32 v3, 0x3fb8aa3b, v3
	v_exp_f32_e32 v3, v3
	v_sub_f32_e32 v0, v0, v80
	v_add_f32_e32 v4, 0, v2
	v_mul_f32_e32 v0, 0x3fb8aa3b, v0
	v_sub_f32_e32 v5, v5, v80
	v_add_f32_e32 v6, v4, v3
	v_exp_f32_e32 v4, v0
	v_mul_f32_e32 v5, 0x3fb8aa3b, v5
	v_exp_f32_e32 v5, v5
	v_add_f32_e32 v0, v6, v4
	v_add_f32_e32 v0, v0, v5
	v_div_scale_f32 v6, s[0:1], v0, v0, 1.0
	v_rcp_f32_e32 v7, v6
	s_nop 0
	v_fma_f32 v9, -v6, v7, 1.0
	v_fmac_f32_e32 v7, v9, v7
	v_div_scale_f32 v9, vcc, 1.0, v0, 1.0
	v_mul_f32_e32 v10, v9, v7
	v_fma_f32 v11, -v6, v10, v9
	v_fmac_f32_e32 v10, v11, v7
	v_fma_f32 v6, -v6, v10, v9
	v_div_fmas_f32 v6, v6, v7, v10
	v_div_fixup_f32 v0, v6, v0, 1.0
	v_lshl_add_u64 v[6:7], s[44:45], 0, v[68:69]
	v_pk_mul_f32 v[4:5], v[4:5], v[0:1] op_sel_hi:[1,0]
	v_pk_mul_f32 v[2:3], v[2:3], v[0:1] op_sel_hi:[1,0]
	v_lshl_add_u64 v[6:7], v[6:7], 4, s[10:11]
	global_store_dwordx4 v[6:7], v[2:5], off
	v_lshl_add_u32 v0, v72, 2, s49
	ds_add_rtn_u32 v0, v0, v170
	v_add_lshl_u32 v2, s86, v68, 4
	v_add_u32_e32 v3, s50, v2
	ds_write_b32 v3, v72
	v_add_u32_e32 v3, s51, v2
	s_waitcnt lgkmcnt(1)
	ds_write_b32 v3, v0
	v_lshl_add_u32 v0, v82, 2, s49
	ds_add_rtn_u32 v0, v0, v170
	v_or_b32_e32 v3, 4, v2
	v_add_u32_e32 v4, s50, v3
	v_add_u32_e32 v3, s51, v3
	ds_write_b32 v4, v82
	s_waitcnt lgkmcnt(1)
	ds_write_b32 v3, v0
	v_lshl_add_u32 v0, v83, 2, s49
	ds_add_rtn_u32 v0, v0, v170
	v_or_b32_e32 v3, 8, v2
	v_add_u32_e32 v4, s50, v3
	v_add_u32_e32 v3, s51, v3
	ds_write_b32 v4, v83
	s_waitcnt lgkmcnt(1)
	ds_write_b32 v3, v0
	v_lshl_add_u32 v0, v8, 2, s49
	ds_add_rtn_u32 v0, v0, v170
	v_or_b32_e32 v2, 12, v2
	v_add_u32_e32 v3, s50, v2
	v_add_u32_e32 v2, s51, v2
	ds_write_b32 v3, v8
	s_waitcnt lgkmcnt(1)
	ds_write_b32 v2, v0
	s_branch .LBB0_590
